# f1/f2 Fourier stages: all DFT-table loads and twiddle gathers of a step issued up front (counted vmcnt waits); router: 8 row loads hoisted, both slot atomics issued back to back
# speedup vs baseline: 1.0771x; 1.0112x over previous
.LBB0_1283:
	v_lshl_add_u64 v[4:5], s[40:41], 0, v[136:137]
	v_add_co_u32_e32 v170, vcc, s27, v4
	s_mov_b32 s18, 0x45000000
	s_nop 0
	v_addc_co_u32_e32 v171, vcc, 0, v5, vcc
	v_add_co_u32_e32 v172, vcc, s97, v4
	s_nop 1
	v_addc_co_u32_e32 v173, vcc, 0, v5, vcc
	global_load_dwordx4 v[180:183], v[170:171], off
	global_load_dwordx4 v[184:187], v[172:173], off
	global_load_dwordx4 v[188:191], v[170:171], off offset:32
	global_load_dwordx4 v[192:195], v[172:173], off offset:32
	global_load_dwordx4 v[196:199], v[170:171], off offset:64
	global_load_dwordx4 v[200:203], v[172:173], off offset:64
	global_load_dwordx4 v[204:207], v[170:171], off offset:96
	global_load_dwordx4 v[208:211], v[172:173], off offset:96
	global_load_dwordx4 v[212:215], v[170:171], off offset:128
	global_load_dwordx4 v[216:219], v[172:173], off offset:128
	global_load_dwordx4 v[232:235], v[170:171], off offset:160
	global_load_dwordx4 v[236:239], v[172:173], off offset:160
	global_load_dwordx4 v[240:243], v[170:171], off offset:192
	global_load_dwordx4 v[244:247], v[172:173], off offset:192
	global_load_dwordx4 v[248:251], v[170:171], off offset:224
	global_load_dwordx4 v[224:227], v[172:173], off offset:224
	s_add_i32 s9, s9, 64
	v_lshl_add_u64 v[136:137], v[136:137], 0, s[14:15]
	s_cmpk_lg_i32 s9, 0x100
	s_waitcnt vmcnt(15)
	v_mfma_f32_32x32x16_bf16 v[0:15], v[32:35], v[180:183], 0
	s_waitcnt vmcnt(14)
	v_mfma_f32_32x32x16_bf16 v[16:31], v[32:35], v[184:187], 0
	s_waitcnt vmcnt(13)
	v_mfma_f32_32x32x16_bf16 v[0:15], v[36:39], v[188:191], v[0:15]
	s_waitcnt vmcnt(12)
	v_mfma_f32_32x32x16_bf16 v[16:31], v[36:39], v[192:195], v[16:31]
	s_waitcnt vmcnt(11)
	v_mfma_f32_32x32x16_bf16 v[0:15], v[40:43], v[196:199], v[0:15]
	s_waitcnt vmcnt(10)
	v_mfma_f32_32x32x16_bf16 v[16:31], v[40:43], v[200:203], v[16:31]
	s_waitcnt vmcnt(9)
	v_mfma_f32_32x32x16_bf16 v[0:15], v[44:47], v[204:207], v[0:15]
	s_waitcnt vmcnt(8)
	v_mfma_f32_32x32x16_bf16 v[16:31], v[44:47], v[208:211], v[16:31]
	v_lshlrev_b32_e32 v161, 2, v176
	global_load_dwordx2 v[180:181], v161, s[0:1]
	global_load_dwordx2 v[182:183], v72, s[40:41]
	global_load_dwordx2 v[184:185], v76, s[40:41]
	global_load_dwordx2 v[186:187], v80, s[40:41]
	global_load_dwordx2 v[188:189], v84, s[40:41]
	global_load_dwordx2 v[190:191], v88, s[40:41]
	global_load_dwordx2 v[192:193], v92, s[40:41]
	global_load_dwordx2 v[194:195], v96, s[40:41]
	global_load_dwordx2 v[196:197], v100, s[40:41]
	global_load_dwordx2 v[198:199], v104, s[40:41]
	global_load_dwordx2 v[200:201], v108, s[40:41]
	global_load_dwordx2 v[202:203], v112, s[40:41]
	global_load_dwordx2 v[204:205], v116, s[40:41]
	global_load_dwordx2 v[206:207], v120, s[40:41]
	global_load_dwordx2 v[208:209], v124, s[40:41]
	global_load_dwordx2 v[210:211], v128, s[40:41]
	s_waitcnt vmcnt(23)
	v_mfma_f32_32x32x16_bf16 v[0:15], v[48:51], v[212:215], v[0:15]
	s_waitcnt vmcnt(22)
	v_mfma_f32_32x32x16_bf16 v[16:31], v[48:51], v[216:219], v[16:31]
	s_waitcnt vmcnt(21)
	v_mfma_f32_32x32x16_bf16 v[0:15], v[52:55], v[232:235], v[0:15]
	s_waitcnt vmcnt(20)
	v_mfma_f32_32x32x16_bf16 v[16:31], v[52:55], v[236:239], v[16:31]
	s_waitcnt vmcnt(19)
	v_mfma_f32_32x32x16_bf16 v[0:15], v[56:59], v[240:243], v[0:15]
	s_waitcnt vmcnt(18)
	v_mfma_f32_32x32x16_bf16 v[16:31], v[56:59], v[244:247], v[16:31]
	s_waitcnt vmcnt(17)
	v_mfma_f32_32x32x16_bf16 v[0:15], v[60:63], v[248:251], v[0:15]
	s_waitcnt vmcnt(16)
	v_mfma_f32_32x32x16_bf16 v[16:31], v[60:63], v[224:227], v[16:31]
	v_lshl_add_u64 v[72:73], v[72:73], 0, v[74:75]
	v_add_u32_e32 v176, v176, v160
	s_nop 7
	s_nop 1
	v_mov_b32_e32 v170, v0
	s_waitcnt vmcnt(12)
	v_mov_b32_e32 v162, v180
	v_mov_b32_e32 v163, v181
	v_mov_b32_e32 v164, v182
	v_mov_b32_e32 v165, v183
	v_mov_b32_e32 v166, v184
	v_mov_b32_e32 v167, v185
	v_mov_b32_e32 v171, v2
	v_mov_b32_e32 v168, v186
	v_mov_b32_e32 v169, v187
	v_mov_b32_e32 v2, v1
	v_lshl_add_u64 v[76:77], v[76:77], 0, v[78:79]
	s_nop 0
	v_mov_b32_e32 v174, v16
	v_mov_b32_e32 v175, v18
	v_mov_b32_e32 v18, v17
	v_lshl_add_u64 v[80:81], v[80:81], 0, v[82:83]
	v_mov_b32_e32 v172, v162
	v_mov_b32_e32 v178, v164
	v_mov_b32_e32 v173, v166
	v_mov_b32_e32 v166, v163
	v_pk_mul_f32 v[162:163], v[174:175], v[166:167]
	v_mov_b32_e32 v179, v168
	v_mov_b32_e32 v168, v165
	v_pk_fma_f32 v[162:163], v[170:171], v[172:173], v[162:163] neg_lo:[0,0,1] neg_hi:[0,0,1]
	v_pk_mul_f32 v[0:1], v[18:19], v[168:169]
	v_and_b32_sdwa v17, v162, v231 dst_sel:DWORD dst_unused:UNUSED_PAD src0_sel:WORD_1 src1_sel:DWORD
	v_pk_fma_f32 v[0:1], v[2:3], v[178:179], v[0:1] neg_lo:[0,0,1] neg_hi:[0,0,1]
	v_add3_u32 v161, v162, v17, s25
	v_and_b32_sdwa v17, v1, v231 dst_sel:DWORD dst_unused:UNUSED_PAD src0_sel:WORD_1 src1_sel:DWORD
	v_and_b32_sdwa v162, v0, v231 dst_sel:DWORD dst_unused:UNUSED_PAD src0_sel:WORD_1 src1_sel:DWORD
	v_and_b32_sdwa v16, v163, v231 dst_sel:DWORD dst_unused:UNUSED_PAD src0_sel:WORD_1 src1_sel:DWORD
	v_add3_u32 v1, v1, v17, s25
	v_add3_u32 v0, v0, v162, s25
	v_add3_u32 v16, v163, v16, s25
	v_and_b32_e32 v1, 0xffff0000, v1
	v_and_b32_e32 v0, 0xffff0000, v0
	v_lshl_add_u64 v[162:163], s[40:41], 0, v[132:133]
	v_or_b32_sdwa v17, v1, v16 dst_sel:DWORD dst_unused:UNUSED_PAD src0_sel:DWORD src1_sel:WORD_1
	v_or_b32_sdwa v16, v0, v161 dst_sel:DWORD dst_unused:UNUSED_PAD src0_sel:DWORD src1_sel:WORD_1
	v_add_co_u32_e32 v0, vcc, s18, v162
	v_pk_mul_f32 v[2:3], v[2:3], v[168:169]
	s_nop 0
	v_addc_co_u32_e32 v1, vcc, 0, v163, vcc
	global_store_dwordx2 v[0:1], v[16:17], off
	v_pk_mul_f32 v[16:17], v[170:171], v[166:167]
	v_pk_fma_f32 v[2:3], v[18:19], v[178:179], v[2:3]
	v_pk_fma_f32 v[16:17], v[174:175], v[172:173], v[16:17]
	s_mov_b32 s18, 0x46000000
	v_and_b32_sdwa v19, v16, v231 dst_sel:DWORD dst_unused:UNUSED_PAD src0_sel:WORD_1 src1_sel:DWORD
	v_and_b32_sdwa v18, v17, v231 dst_sel:DWORD dst_unused:UNUSED_PAD src0_sel:WORD_1 src1_sel:DWORD
	v_add3_u32 v16, v16, v19, s25
	v_and_b32_sdwa v19, v2, v231 dst_sel:DWORD dst_unused:UNUSED_PAD src0_sel:WORD_1 src1_sel:DWORD
	v_add3_u32 v17, v17, v18, s25
	v_and_b32_sdwa v18, v3, v231 dst_sel:DWORD dst_unused:UNUSED_PAD src0_sel:WORD_1 src1_sel:DWORD
	v_add3_u32 v2, v2, v19, s25
	v_add3_u32 v3, v3, v18, s25
	v_and_b32_e32 v2, 0xffff0000, v2
	v_and_b32_e32 v3, 0xffff0000, v3
	v_or_b32_sdwa v2, v2, v16 dst_sel:DWORD dst_unused:UNUSED_PAD src0_sel:DWORD src1_sel:WORD_1
	v_add_co_u32_e32 v16, vcc, s18, v162
	v_or_b32_sdwa v3, v3, v17 dst_sel:DWORD dst_unused:UNUSED_PAD src0_sel:DWORD src1_sel:WORD_1
	s_nop 0
	v_addc_co_u32_e32 v17, vcc, 0, v163, vcc
	global_store_dwordx2 v[16:17], v[2:3], off
	s_waitcnt vmcnt(10)
	v_mov_b32_e32 v2, v188
	v_mov_b32_e32 v3, v189
	v_mov_b32_e32 v16, v190
	v_mov_b32_e32 v17, v191
	v_mov_b32_e32 v18, v192
	v_mov_b32_e32 v19, v193
	v_mov_b32_e32 v168, v20
	v_mov_b32_e32 v162, v194
	v_mov_b32_e32 v163, v195
	v_mov_b32_e32 v169, v22
	v_mov_b32_e32 v164, v4
	v_mov_b32_e32 v165, v6
	v_mov_b32_e32 v6, v5
	v_mov_b32_e32 v22, v21
	v_lshl_add_u64 v[132:133], v[132:133], 0, s[6:7]
	v_lshl_add_u64 v[84:85], v[84:85], 0, v[86:87]
	v_lshl_add_u64 v[88:89], v[88:89], 0, v[90:91]
	v_lshl_add_u64 v[92:93], v[92:93], 0, v[94:95]
	v_lshl_add_u64 v[96:97], v[96:97], 0, v[98:99]
	v_mov_b32_e32 v166, v2
	v_mov_b32_e32 v4, v16
	v_mov_b32_e32 v167, v18
	v_mov_b32_e32 v18, v3
	v_pk_mul_f32 v[2:3], v[168:169], v[18:19]
	v_mov_b32_e32 v5, v162
	v_mov_b32_e32 v162, v17
	v_pk_fma_f32 v[2:3], v[164:165], v[166:167], v[2:3] neg_lo:[0,0,1] neg_hi:[0,0,1]
	v_pk_mul_f32 v[16:17], v[22:23], v[162:163]
	v_and_b32_sdwa v20, v3, v231 dst_sel:DWORD dst_unused:UNUSED_PAD src0_sel:WORD_1 src1_sel:DWORD
	v_pk_fma_f32 v[16:17], v[6:7], v[4:5], v[16:17] neg_lo:[0,0,1] neg_hi:[0,0,1]
	v_and_b32_sdwa v21, v2, v231 dst_sel:DWORD dst_unused:UNUSED_PAD src0_sel:WORD_1 src1_sel:DWORD
	v_add3_u32 v2, v2, v21, s25
	v_add3_u32 v3, v3, v20, s25
	v_and_b32_sdwa v20, v17, v231 dst_sel:DWORD dst_unused:UNUSED_PAD src0_sel:WORD_1 src1_sel:DWORD
	v_and_b32_sdwa v21, v16, v231 dst_sel:DWORD dst_unused:UNUSED_PAD src0_sel:WORD_1 src1_sel:DWORD
	v_add3_u32 v17, v17, v20, s25
	v_add3_u32 v16, v16, v21, s25
	v_and_b32_e32 v17, 0xffff0000, v17
	v_and_b32_e32 v16, 0xffff0000, v16
	v_or_b32_sdwa v3, v17, v3 dst_sel:DWORD dst_unused:UNUSED_PAD src0_sel:DWORD src1_sel:WORD_1
	v_or_b32_sdwa v2, v16, v2 dst_sel:DWORD dst_unused:UNUSED_PAD src0_sel:DWORD src1_sel:WORD_1
	global_store_dwordx2 v[0:1], v[2:3], off offset:16
	v_pk_mul_f32 v[2:3], v[164:165], v[18:19]
	v_pk_mul_f32 v[6:7], v[6:7], v[162:163]
	v_pk_fma_f32 v[2:3], v[168:169], v[166:167], v[2:3]
	v_pk_fma_f32 v[4:5], v[22:23], v[4:5], v[6:7]
	v_and_b32_sdwa v6, v3, v231 dst_sel:DWORD dst_unused:UNUSED_PAD src0_sel:WORD_1 src1_sel:DWORD
	v_and_b32_sdwa v7, v2, v231 dst_sel:DWORD dst_unused:UNUSED_PAD src0_sel:WORD_1 src1_sel:DWORD
	v_add3_u32 v2, v2, v7, s25
	v_add3_u32 v3, v3, v6, s25
	v_and_b32_sdwa v6, v5, v231 dst_sel:DWORD dst_unused:UNUSED_PAD src0_sel:WORD_1 src1_sel:DWORD
	v_and_b32_sdwa v7, v4, v231 dst_sel:DWORD dst_unused:UNUSED_PAD src0_sel:WORD_1 src1_sel:DWORD
	v_add3_u32 v5, v5, v6, s25
	v_add3_u32 v4, v4, v7, s25
	v_and_b32_e32 v5, 0xffff0000, v5
	v_and_b32_e32 v4, 0xffff0000, v4
	v_or_b32_sdwa v5, v5, v3 dst_sel:DWORD dst_unused:UNUSED_PAD src0_sel:DWORD src1_sel:WORD_1
	v_or_b32_sdwa v4, v4, v2 dst_sel:DWORD dst_unused:UNUSED_PAD src0_sel:DWORD src1_sel:WORD_1
	v_lshl_add_u64 v[2:3], s[40:41], 0, v[134:135]
	global_store_dwordx2 v[2:3], v[4:5], off
	s_waitcnt vmcnt(8)
	v_mov_b32_e32 v16, v196
	v_mov_b32_e32 v17, v197
	v_mov_b32_e32 v18, v198
	v_mov_b32_e32 v19, v199
	v_mov_b32_e32 v6, v200
	v_mov_b32_e32 v7, v201
	v_mov_b32_e32 v20, v8
	v_mov_b32_e32 v4, v202
	v_mov_b32_e32 v5, v203
	v_mov_b32_e32 v21, v10
	v_mov_b32_e32 v162, v24
	v_mov_b32_e32 v163, v26
	v_mov_b32_e32 v10, v9
	v_mov_b32_e32 v26, v25
	v_lshl_add_u64 v[134:135], v[134:135], 0, s[6:7]
	v_lshl_add_u64 v[100:101], v[100:101], 0, v[102:103]
	v_lshl_add_u64 v[104:105], v[104:105], 0, v[106:107]
	v_lshl_add_u64 v[108:109], v[108:109], 0, v[110:111]
	v_lshl_add_u64 v[112:113], v[112:113], 0, v[114:115]
	v_mov_b32_e32 v22, v16
	v_mov_b32_e32 v8, v18
	v_mov_b32_e32 v23, v6
	v_mov_b32_e32 v6, v17
	v_pk_mul_f32 v[16:17], v[162:163], v[6:7]
	v_mov_b32_e32 v9, v4
	v_mov_b32_e32 v4, v19
	v_pk_mul_f32 v[6:7], v[20:21], v[6:7]
	v_pk_fma_f32 v[16:17], v[20:21], v[22:23], v[16:17] neg_lo:[0,0,1] neg_hi:[0,0,1]
	v_pk_mul_f32 v[18:19], v[26:27], v[4:5]
	v_pk_fma_f32 v[6:7], v[162:163], v[22:23], v[6:7]
	v_pk_mul_f32 v[4:5], v[10:11], v[4:5]
	v_pk_fma_f32 v[18:19], v[10:11], v[8:9], v[18:19] neg_lo:[0,0,1] neg_hi:[0,0,1]
	v_and_b32_sdwa v24, v17, v231 dst_sel:DWORD dst_unused:UNUSED_PAD src0_sel:WORD_1 src1_sel:DWORD
	v_and_b32_sdwa v25, v16, v231 dst_sel:DWORD dst_unused:UNUSED_PAD src0_sel:WORD_1 src1_sel:DWORD
	v_pk_fma_f32 v[4:5], v[26:27], v[8:9], v[4:5]
	v_and_b32_sdwa v8, v7, v231 dst_sel:DWORD dst_unused:UNUSED_PAD src0_sel:WORD_1 src1_sel:DWORD
	v_and_b32_sdwa v9, v6, v231 dst_sel:DWORD dst_unused:UNUSED_PAD src0_sel:WORD_1 src1_sel:DWORD
	v_add3_u32 v16, v16, v25, s25
	v_add3_u32 v17, v17, v24, s25
	v_and_b32_sdwa v24, v19, v231 dst_sel:DWORD dst_unused:UNUSED_PAD src0_sel:WORD_1 src1_sel:DWORD
	v_and_b32_sdwa v25, v18, v231 dst_sel:DWORD dst_unused:UNUSED_PAD src0_sel:WORD_1 src1_sel:DWORD
	v_add3_u32 v6, v6, v9, s25
	v_add3_u32 v7, v7, v8, s25
	v_and_b32_sdwa v8, v5, v231 dst_sel:DWORD dst_unused:UNUSED_PAD src0_sel:WORD_1 src1_sel:DWORD
	v_and_b32_sdwa v9, v4, v231 dst_sel:DWORD dst_unused:UNUSED_PAD src0_sel:WORD_1 src1_sel:DWORD
	v_add3_u32 v19, v19, v24, s25
	v_add3_u32 v18, v18, v25, s25
	v_add3_u32 v5, v5, v8, s25
	v_add3_u32 v4, v4, v9, s25
	v_and_b32_e32 v19, 0xffff0000, v19
	v_and_b32_e32 v18, 0xffff0000, v18
	v_and_b32_e32 v5, 0xffff0000, v5
	v_and_b32_e32 v4, 0xffff0000, v4
	v_or_b32_sdwa v17, v19, v17 dst_sel:DWORD dst_unused:UNUSED_PAD src0_sel:DWORD src1_sel:WORD_1
	v_or_b32_sdwa v16, v18, v16 dst_sel:DWORD dst_unused:UNUSED_PAD src0_sel:DWORD src1_sel:WORD_1
	v_or_b32_sdwa v5, v5, v7 dst_sel:DWORD dst_unused:UNUSED_PAD src0_sel:DWORD src1_sel:WORD_1
	v_or_b32_sdwa v4, v4, v6 dst_sel:DWORD dst_unused:UNUSED_PAD src0_sel:DWORD src1_sel:WORD_1
	global_store_dwordx2 v[0:1], v[16:17], off offset:32
	global_store_dwordx2 v[2:3], v[4:5], off offset:16
	s_waitcnt vmcnt(6)
	v_mov_b32_e32 v4, v204
	v_mov_b32_e32 v5, v205
	v_mov_b32_e32 v6, v206
	v_mov_b32_e32 v7, v207
	v_mov_b32_e32 v8, v208
	v_mov_b32_e32 v9, v209
	v_mov_b32_e32 v20, v28
	v_mov_b32_e32 v10, v210
	v_mov_b32_e32 v11, v211
	v_mov_b32_e32 v21, v30
	v_mov_b32_e32 v16, v12
	v_mov_b32_e32 v17, v14
	v_mov_b32_e32 v14, v13
	v_mov_b32_e32 v30, v29
	v_lshl_add_u64 v[116:117], v[116:117], 0, v[118:119]
	v_lshl_add_u64 v[120:121], v[120:121], 0, v[122:123]
	v_lshl_add_u64 v[124:125], v[124:125], 0, v[126:127]
	v_lshl_add_u64 v[128:129], v[128:129], 0, v[130:131]
	v_mov_b32_e32 v18, v4
	v_mov_b32_e32 v12, v6
	v_mov_b32_e32 v19, v8
	v_mov_b32_e32 v8, v5
	v_pk_mul_f32 v[4:5], v[20:21], v[8:9]
	v_mov_b32_e32 v13, v10
	v_mov_b32_e32 v10, v7
	v_pk_fma_f32 v[4:5], v[16:17], v[18:19], v[4:5] neg_lo:[0,0,1] neg_hi:[0,0,1]
	v_pk_mul_f32 v[6:7], v[30:31], v[10:11]
	v_and_b32_sdwa v22, v5, v231 dst_sel:DWORD dst_unused:UNUSED_PAD src0_sel:WORD_1 src1_sel:DWORD
	v_pk_fma_f32 v[6:7], v[14:15], v[12:13], v[6:7] neg_lo:[0,0,1] neg_hi:[0,0,1]
	v_and_b32_sdwa v23, v4, v231 dst_sel:DWORD dst_unused:UNUSED_PAD src0_sel:WORD_1 src1_sel:DWORD
	v_add3_u32 v4, v4, v23, s25
	v_add3_u32 v5, v5, v22, s25
	v_and_b32_sdwa v22, v7, v231 dst_sel:DWORD dst_unused:UNUSED_PAD src0_sel:WORD_1 src1_sel:DWORD
	v_and_b32_sdwa v23, v6, v231 dst_sel:DWORD dst_unused:UNUSED_PAD src0_sel:WORD_1 src1_sel:DWORD
	v_add3_u32 v7, v7, v22, s25
	v_add3_u32 v6, v6, v23, s25
	v_and_b32_e32 v7, 0xffff0000, v7
	v_and_b32_e32 v6, 0xffff0000, v6
	v_or_b32_sdwa v5, v7, v5 dst_sel:DWORD dst_unused:UNUSED_PAD src0_sel:DWORD src1_sel:WORD_1
	v_or_b32_sdwa v4, v6, v4 dst_sel:DWORD dst_unused:UNUSED_PAD src0_sel:DWORD src1_sel:WORD_1
	global_store_dwordx2 v[0:1], v[4:5], off offset:48
	v_pk_mul_f32 v[0:1], v[16:17], v[8:9]
	v_pk_mul_f32 v[4:5], v[14:15], v[10:11]
	v_pk_fma_f32 v[0:1], v[20:21], v[18:19], v[0:1]
	v_pk_fma_f32 v[4:5], v[30:31], v[12:13], v[4:5]
	v_and_b32_sdwa v6, v1, v231 dst_sel:DWORD dst_unused:UNUSED_PAD src0_sel:WORD_1 src1_sel:DWORD
	v_and_b32_sdwa v7, v0, v231 dst_sel:DWORD dst_unused:UNUSED_PAD src0_sel:WORD_1 src1_sel:DWORD
	v_add3_u32 v0, v0, v7, s25
	v_add3_u32 v1, v1, v6, s25
	v_and_b32_sdwa v6, v5, v231 dst_sel:DWORD dst_unused:UNUSED_PAD src0_sel:WORD_1 src1_sel:DWORD
	v_and_b32_sdwa v7, v4, v231 dst_sel:DWORD dst_unused:UNUSED_PAD src0_sel:WORD_1 src1_sel:DWORD
	v_add3_u32 v5, v5, v6, s25
	v_add3_u32 v4, v4, v7, s25
	v_and_b32_e32 v5, 0xffff0000, v5
	v_and_b32_e32 v4, 0xffff0000, v4
	v_or_b32_sdwa v1, v5, v1 dst_sel:DWORD dst_unused:UNUSED_PAD src0_sel:DWORD src1_sel:WORD_1
	v_or_b32_sdwa v0, v4, v0 dst_sel:DWORD dst_unused:UNUSED_PAD src0_sel:DWORD src1_sel:WORD_1
	global_store_dwordx2 v[2:3], v[0:1], off offset:32
	s_cbranch_scc1 .LBB0_1283
	s_add_i32 s8, s8, s5
	s_add_i32 s2, s2, s3
	s_cmpk_gt_i32 s8, 0x7ff
	s_cbranch_scc0 .LBB0_1282

.LBB0_1319:
	v_lshl_add_u64 v[114:115], s[40:41], 0, v[106:107]
	v_add_co_u32_e32 v116, vcc, 0x108000, v114
	s_add_i32 s2, s2, -1
	s_nop 0
	v_addc_co_u32_e32 v117, vcc, 0, v115, vcc
	v_add_co_u32_e32 v118, vcc, s27, v114
	s_mov_b64 s[8:9], 0x1400000
	s_nop 0
	v_addc_co_u32_e32 v119, vcc, 0, v115, vcc
	global_load_dwordx4 v[132:135], v[116:117], off
	global_load_dwordx4 v[136:139], v[116:117], off offset:32
	global_load_dwordx4 v[140:143], v[116:117], off offset:64
	global_load_dwordx4 v[144:147], v[116:117], off offset:96
	global_load_dwordx4 v[148:151], v[116:117], off offset:128
	global_load_dwordx4 v[152:155], v[116:117], off offset:160
	global_load_dwordx4 v[156:159], v[116:117], off offset:192
	global_load_dwordx4 v[160:163], v[116:117], off offset:224
	global_load_dwordx4 v[164:167], v[118:119], off
	global_load_dwordx4 v[168:171], v[118:119], off offset:32
	global_load_dwordx4 v[172:175], v[118:119], off offset:64
	global_load_dwordx4 v[180:183], v[118:119], off offset:96
	global_load_dwordx4 v[184:187], v[118:119], off offset:128
	global_load_dwordx4 v[192:195], v[118:119], off offset:160
	global_load_dwordx4 v[196:199], v[118:119], off offset:192
	global_load_dwordx4 v[200:203], v[118:119], off offset:224
	v_lshl_add_u64 v[106:107], v[106:107], 0, s[14:15]
	s_cmp_lg_u32 s2, 0
	s_waitcnt vmcnt(15)
	v_mfma_f32_32x32x16_bf16 v[16:31], v[40:43], v[132:135], 0
	v_mfma_f32_32x32x16_bf16 v[0:15], v[32:35], v[132:135], 0
	s_waitcnt vmcnt(14)
	v_mfma_f32_32x32x16_bf16 v[16:31], v[44:47], v[136:139], v[16:31]
	v_mfma_f32_32x32x16_bf16 v[0:15], v[36:39], v[136:139], v[0:15]
	s_waitcnt vmcnt(13)
	v_mfma_f32_32x32x16_bf16 v[16:31], v[56:59], v[140:143], v[16:31]
	v_mfma_f32_32x32x16_bf16 v[0:15], v[48:51], v[140:143], v[0:15]
	s_waitcnt vmcnt(12)
	v_mfma_f32_32x32x16_bf16 v[16:31], v[60:63], v[144:147], v[16:31]
	v_mfma_f32_32x32x16_bf16 v[0:15], v[52:55], v[144:147], v[0:15]
	s_waitcnt vmcnt(11)
	v_mfma_f32_32x32x16_bf16 v[16:31], v[72:75], v[148:151], v[16:31]
	v_mfma_f32_32x32x16_bf16 v[0:15], v[64:67], v[148:151], v[0:15]
	s_waitcnt vmcnt(10)
	v_mfma_f32_32x32x16_bf16 v[16:31], v[76:79], v[152:155], v[16:31]
	v_mfma_f32_32x32x16_bf16 v[0:15], v[68:71], v[152:155], v[0:15]
	s_waitcnt vmcnt(9)
	v_mfma_f32_32x32x16_bf16 v[16:31], v[88:91], v[156:159], v[16:31]
	v_mfma_f32_32x32x16_bf16 v[0:15], v[80:83], v[156:159], v[0:15]
	s_waitcnt vmcnt(8)
	v_mfma_f32_32x32x16_bf16 v[16:31], v[92:95], v[160:163], v[16:31]
	s_nop 11
	v_xor_b32_e32 v31, 0x80000000, v31
	v_mfma_f32_32x32x16_bf16 v[0:15], v[84:87], v[160:163], v[0:15]
	v_xor_b32_e32 v30, 0x80000000, v30
	v_xor_b32_e32 v29, 0x80000000, v29
	v_xor_b32_e32 v28, 0x80000000, v28
	v_xor_b32_e32 v27, 0x80000000, v27
	v_xor_b32_e32 v26, 0x80000000, v26
	v_xor_b32_e32 v25, 0x80000000, v25
	v_xor_b32_e32 v24, 0x80000000, v24
	v_xor_b32_e32 v23, 0x80000000, v23
	v_xor_b32_e32 v22, 0x80000000, v22
	v_xor_b32_e32 v21, 0x80000000, v21
	v_xor_b32_e32 v20, 0x80000000, v20
	v_xor_b32_e32 v19, 0x80000000, v19
	v_xor_b32_e32 v18, 0x80000000, v18
	v_xor_b32_e32 v17, 0x80000000, v17
	v_xor_b32_e32 v16, 0x80000000, v16
	s_waitcnt vmcnt(7)
	v_mfma_f32_32x32x16_bf16 v[0:15], v[40:43], v[164:167], v[0:15]
	v_mfma_f32_32x32x16_bf16 v[16:31], v[32:35], v[164:167], v[16:31]
	v_lshl_add_u64 v[114:115], s[40:41], 0, v[104:105]
	v_lshl_add_u64 v[104:105], v[104:105], 0, s[8:9]
	s_waitcnt vmcnt(6)
	v_mfma_f32_32x32x16_bf16 v[0:15], v[44:47], v[168:171], v[0:15]
	v_mfma_f32_32x32x16_bf16 v[16:31], v[36:39], v[168:171], v[16:31]
	s_waitcnt vmcnt(5)
	v_mfma_f32_32x32x16_bf16 v[0:15], v[56:59], v[172:175], v[0:15]
	v_mfma_f32_32x32x16_bf16 v[16:31], v[48:51], v[172:175], v[16:31]
	s_waitcnt vmcnt(4)
	v_mfma_f32_32x32x16_bf16 v[0:15], v[60:63], v[180:183], v[0:15]
	v_mfma_f32_32x32x16_bf16 v[16:31], v[52:55], v[180:183], v[16:31]
	s_waitcnt vmcnt(3)
	v_mfma_f32_32x32x16_bf16 v[0:15], v[72:75], v[184:187], v[0:15]
	v_mfma_f32_32x32x16_bf16 v[16:31], v[64:67], v[184:187], v[16:31]
	s_waitcnt vmcnt(2)
	v_mfma_f32_32x32x16_bf16 v[0:15], v[76:79], v[192:195], v[0:15]
	v_mfma_f32_32x32x16_bf16 v[16:31], v[68:71], v[192:195], v[16:31]
	s_waitcnt vmcnt(1)
	v_mfma_f32_32x32x16_bf16 v[0:15], v[88:91], v[196:199], v[0:15]
	v_mfma_f32_32x32x16_bf16 v[16:31], v[80:83], v[196:199], v[16:31]
	s_waitcnt vmcnt(0)
	v_mfma_f32_32x32x16_bf16 v[0:15], v[92:95], v[200:203], v[0:15]
	s_nop 11
	v_bfe_u32 v116, v4, 16, 1
	v_mfma_f32_32x32x16_bf16 v[16:31], v[84:87], v[200:203], v[16:31]
	v_bfe_u32 v110, v0, 16, 1
	v_bfe_u32 v112, v2, 16, 1
	v_bfe_u32 v118, v6, 16, 1
	v_bfe_u32 v120, v8, 16, 1
	v_bfe_u32 v122, v10, 16, 1
	v_bfe_u32 v124, v12, 16, 1
	v_bfe_u32 v126, v14, 16, 1
	v_bfe_u32 v111, v1, 16, 1
	v_bfe_u32 v113, v3, 16, 1
	v_bfe_u32 v117, v5, 16, 1
	v_bfe_u32 v119, v7, 16, 1
	v_bfe_u32 v121, v9, 16, 1
	v_bfe_u32 v123, v11, 16, 1
	v_bfe_u32 v125, v13, 16, 1
	v_bfe_u32 v127, v15, 16, 1
	v_bfe_u32 v128, v16, 16, 1
	v_bfe_u32 v130, v18, 16, 1
	v_add3_u32 v0, v0, v110, s25
	v_add3_u32 v2, v2, v112, s25
	v_bfe_u32 v110, v20, 16, 1
	v_bfe_u32 v112, v22, 16, 1
	v_add3_u32 v4, v4, v116, s25
	v_add3_u32 v6, v6, v118, s25
	v_bfe_u32 v116, v24, 16, 1
	v_bfe_u32 v118, v26, 16, 1
	v_add3_u32 v8, v8, v120, s25
	v_add3_u32 v10, v10, v122, s25
	v_bfe_u32 v120, v28, 16, 1
	v_bfe_u32 v122, v30, 16, 1
	v_add3_u32 v12, v12, v124, s25
	v_add3_u32 v14, v14, v126, s25
	v_bfe_u32 v129, v17, 16, 1
	v_bfe_u32 v131, v19, 16, 1
	v_add3_u32 v1, v1, v111, s25
	v_add3_u32 v3, v3, v113, s25
	v_bfe_u32 v111, v21, 16, 1
	v_bfe_u32 v113, v23, 16, 1
	v_add3_u32 v5, v5, v117, s25
	v_add3_u32 v7, v7, v119, s25
	v_bfe_u32 v117, v25, 16, 1
	v_bfe_u32 v119, v27, 16, 1
	v_add3_u32 v9, v9, v121, s25
	v_add3_u32 v11, v11, v123, s25
	v_bfe_u32 v121, v29, 16, 1
	v_bfe_u32 v123, v31, 16, 1
	v_add3_u32 v13, v13, v125, s25
	v_add3_u32 v15, v15, v127, s25
	v_add3_u32 v16, v16, v128, s25
	v_add3_u32 v18, v18, v130, s25
	v_lshrrev_b32_e32 v0, 16, v0
	v_lshrrev_b32_e32 v2, 16, v2
	v_add3_u32 v20, v20, v110, s25
	v_add3_u32 v22, v22, v112, s25
	v_lshrrev_b32_e32 v4, 16, v4
	v_lshrrev_b32_e32 v6, 16, v6
	v_add3_u32 v24, v24, v116, s25
	v_add3_u32 v26, v26, v118, s25
	v_lshrrev_b32_e32 v8, 16, v8
	v_lshrrev_b32_e32 v10, 16, v10
	v_add3_u32 v28, v28, v120, s25
	v_add3_u32 v30, v30, v122, s25
	v_lshrrev_b32_e32 v12, 16, v12
	v_lshrrev_b32_e32 v14, 16, v14
	v_add3_u32 v17, v17, v129, s25
	v_add3_u32 v19, v19, v131, s25
	v_add3_u32 v21, v21, v111, s25
	v_add3_u32 v23, v23, v113, s25
	v_add3_u32 v25, v25, v117, s25
	v_add3_u32 v27, v27, v119, s25
	v_add3_u32 v29, v29, v121, s25
	v_add3_u32 v31, v31, v123, s25
	v_lshrrev_b32_e32 v16, 16, v16
	v_lshrrev_b32_e32 v18, 16, v18
	v_and_or_b32 v0, v1, s10, v0
	v_and_or_b32 v1, v3, s10, v2
	v_lshrrev_b32_e32 v20, 16, v20
	v_lshrrev_b32_e32 v22, 16, v22
	v_and_or_b32 v2, v5, s10, v4
	v_and_or_b32 v3, v7, s10, v6
	v_lshrrev_b32_e32 v24, 16, v24
	v_lshrrev_b32_e32 v26, 16, v26
	v_and_or_b32 v4, v9, s10, v8
	v_and_or_b32 v5, v11, s10, v10
	v_lshrrev_b32_e32 v10, 16, v28
	v_lshrrev_b32_e32 v11, 16, v30
	v_and_or_b32 v6, v13, s10, v12
	v_and_or_b32 v7, v15, s10, v14
	v_and_or_b32 v8, v17, s10, v16
	v_and_or_b32 v9, v19, s10, v18
	global_store_dwordx2 v[114:115], v[0:1], off
	v_and_or_b32 v0, v21, s10, v20
	v_and_or_b32 v1, v23, s10, v22
	global_store_dwordx2 v[114:115], v[2:3], off offset:16
	v_and_or_b32 v2, v25, s10, v24
	v_and_or_b32 v3, v27, s10, v26
	global_store_dwordx2 v[114:115], v[4:5], off offset:32
	v_and_or_b32 v4, v29, s10, v10
	v_and_or_b32 v5, v31, s10, v11
	global_store_dwordx2 v[114:115], v[6:7], off offset:48
	global_store_dwordx2 v[114:115], v[8:9], off offset:-1024
	global_store_dwordx2 v[114:115], v[0:1], off offset:-1008
	global_store_dwordx2 v[114:115], v[2:3], off offset:-992
	global_store_dwordx2 v[114:115], v[4:5], off offset:-976
	s_cbranch_scc1 .LBB0_1319
	s_add_i32 s4, s4, s5
	s_add_i32 s0, s0, s1
	s_cmpk_lt_i32 s4, 0x800
	s_cbranch_scc1 .LBB0_1318

.LBB0_1622:
	v_lshl_add_u64 v[0:1], s[52:53], 0, v[18:19]
	s_waitcnt lgkmcnt(0)
	v_add_co_u32_e32 v20, vcc, 0x2d000000, v0
	s_nop 1
	v_addc_co_u32_e32 v21, vcc, 0, v1, vcc
	global_load_dwordx2 v[60:61], v[20:21], off
	global_load_dwordx2 v[62:63], v[20:21], off offset:512
	global_load_dwordx2 v[64:65], v[20:21], off offset:1024
	global_load_dwordx2 v[66:67], v[20:21], off offset:1536
	global_load_dwordx2 v[68:69], v[20:21], off offset:2048
	global_load_dwordx2 v[70:71], v[20:21], off offset:2560
	global_load_dwordx2 v[72:73], v[20:21], off offset:3072
	global_load_dwordx2 v[74:75], v[20:21], off offset:3584
	s_waitcnt vmcnt(7)
	v_mov_b32_e32 v0, v60
	v_mov_b32_e32 v1, v61
	v_lshlrev_b32_e32 v26, 16, v0
	v_and_b32_e32 v28, 0xffff0000, v0
	v_lshlrev_b32_e32 v30, 16, v1
	v_and_b32_e32 v32, 0xffff0000, v1
	ds_read_b128 v[0:3], v25
	ds_read_b128 v[4:7], v25 offset:32768
	v_mul_f32_e32 v40, v28, v28
	v_fmac_f32_e32 v40, v26, v26
	v_fmac_f32_e32 v40, v30, v30
	s_waitcnt lgkmcnt(1)
	v_fma_f32 v39, v2, v26, 0
	v_fma_f32 v37, v3, v26, 0
	s_waitcnt lgkmcnt(0)
	v_fma_f32 v35, v4, v26, 0
	v_fma_f32 v33, v5, v26, 0
	v_fma_f32 v31, v6, v26, 0
	v_fma_f32 v29, v7, v26, 0
	ds_read_b128 v[2:5], v25 offset:8192
	ds_read_b128 v[6:9], v25 offset:40960
	v_pk_fma_f32 v[0:1], v[0:1], v[26:27], 0 op_sel_hi:[1,0,0]
	v_fmac_f32_e32 v40, v32, v32
	s_waitcnt lgkmcnt(1)
	v_fmac_f32_e32 v39, v4, v28
	v_fmac_f32_e32 v37, v5, v28
	s_waitcnt lgkmcnt(0)
	v_fmac_f32_e32 v35, v6, v28
	v_fmac_f32_e32 v33, v7, v28
	v_fmac_f32_e32 v31, v8, v28
	v_fmac_f32_e32 v29, v9, v28
	ds_read_b128 v[4:7], v25 offset:16384
	ds_read_b128 v[8:11], v25 offset:49152
	s_waitcnt lgkmcnt(1)
	v_fmac_f32_e32 v39, v6, v30
	v_fmac_f32_e32 v37, v7, v30
	s_waitcnt lgkmcnt(0)
	v_fmac_f32_e32 v35, v8, v30
	v_fmac_f32_e32 v33, v9, v30
	v_fmac_f32_e32 v31, v10, v30
	v_fmac_f32_e32 v29, v11, v30
	ds_read_b128 v[6:9], v25 offset:24576
	ds_read_b128 v[10:13], v25 offset:57344
	s_waitcnt lgkmcnt(1)
	v_fmac_f32_e32 v39, v8, v32
	v_fmac_f32_e32 v37, v9, v32
	s_waitcnt lgkmcnt(0)
	v_fmac_f32_e32 v35, v10, v32
	v_fmac_f32_e32 v33, v11, v32
	v_fmac_f32_e32 v31, v12, v32
	v_fmac_f32_e32 v29, v13, v32
	v_pk_fma_f32 v[0:1], v[2:3], v[28:29], v[0:1] op_sel_hi:[1,0,1]
	s_waitcnt vmcnt(6)
	v_mov_b32_e32 v8, v62
	v_mov_b32_e32 v9, v63
	v_lshlrev_b32_e32 v34, 16, v8
	v_and_b32_e32 v16, 0xffff0000, v8
	v_lshlrev_b32_e32 v22, 16, v9
	v_and_b32_e32 v24, 0xffff0000, v9
	ds_read_b128 v[8:11], v25 offset:1024
	ds_read_b128 v[12:15], v25 offset:33792
	v_pk_fma_f32 v[0:1], v[4:5], v[30:31], v[0:1] op_sel_hi:[1,0,1]
	v_fmac_f32_e32 v40, v34, v34
	v_pk_fma_f32 v[0:1], v[6:7], v[32:33], v[0:1] op_sel_hi:[1,0,1]
	s_waitcnt lgkmcnt(1)
	v_fmac_f32_e32 v39, v10, v34
	v_pk_fma_f32 v[26:27], v[8:9], v[34:35], v[0:1] op_sel_hi:[1,0,1]
	ds_read_b128 v[0:3], v25 offset:9216
	ds_read_b128 v[4:7], v25 offset:41984
	v_fmac_f32_e32 v37, v11, v34
	s_waitcnt lgkmcnt(2)
	v_fmac_f32_e32 v35, v12, v34
	v_fmac_f32_e32 v33, v13, v34
	v_fmac_f32_e32 v31, v14, v34
	v_fmac_f32_e32 v29, v15, v34
	s_waitcnt lgkmcnt(1)
	v_fmac_f32_e32 v39, v2, v16
	v_fmac_f32_e32 v37, v3, v16
	s_waitcnt lgkmcnt(0)
	v_fmac_f32_e32 v35, v4, v16
	v_fmac_f32_e32 v33, v5, v16
	v_fmac_f32_e32 v31, v6, v16
	v_fmac_f32_e32 v29, v7, v16
	ds_read_b128 v[2:5], v25 offset:17408
	ds_read_b128 v[6:9], v25 offset:50176
	v_pk_fma_f32 v[0:1], v[0:1], v[16:17], v[26:27] op_sel_hi:[1,0,1]
	v_fmac_f32_e32 v40, v16, v16
	v_fmac_f32_e32 v40, v22, v22
	s_waitcnt lgkmcnt(1)
	v_fmac_f32_e32 v39, v4, v22
	v_fmac_f32_e32 v37, v5, v22
	s_waitcnt lgkmcnt(0)
	v_fmac_f32_e32 v35, v6, v22
	v_fmac_f32_e32 v33, v7, v22
	v_fmac_f32_e32 v31, v8, v22
	v_fmac_f32_e32 v29, v9, v22
	ds_read_b128 v[4:7], v25 offset:25600
	ds_read_b128 v[8:11], v25 offset:58368
	v_pk_fma_f32 v[0:1], v[2:3], v[22:23], v[0:1] op_sel_hi:[1,0,1]
	v_fmac_f32_e32 v40, v24, v24
	s_waitcnt lgkmcnt(1)
	v_fmac_f32_e32 v39, v6, v24
	v_fmac_f32_e32 v37, v7, v24
	s_waitcnt lgkmcnt(0)
	v_fmac_f32_e32 v35, v8, v24
	v_fmac_f32_e32 v33, v9, v24
	v_fmac_f32_e32 v31, v10, v24
	v_fmac_f32_e32 v29, v11, v24
	v_pk_fma_f32 v[0:1], v[4:5], v[24:25], v[0:1] op_sel_hi:[1,0,1]
	s_waitcnt vmcnt(5)
	v_mov_b32_e32 v6, v64
	v_mov_b32_e32 v7, v65
	v_lshlrev_b32_e32 v28, 16, v6
	v_and_b32_e32 v30, 0xffff0000, v6
	v_lshlrev_b32_e32 v32, 16, v7
	v_and_b32_e32 v34, 0xffff0000, v7
	ds_read_b128 v[6:9], v25 offset:2048
	ds_read_b128 v[10:13], v25 offset:34816
	v_fmac_f32_e32 v40, v28, v28
	v_fmac_f32_e32 v40, v30, v30
	v_fmac_f32_e32 v40, v32, v32
	s_waitcnt lgkmcnt(1)
	v_fmac_f32_e32 v39, v8, v28
	v_fmac_f32_e32 v37, v9, v28
	s_waitcnt lgkmcnt(0)
	v_fmac_f32_e32 v35, v10, v28
	v_fmac_f32_e32 v33, v11, v28
	v_fmac_f32_e32 v31, v12, v28
	v_fmac_f32_e32 v29, v13, v28
	ds_read_b128 v[8:11], v25 offset:10240
	ds_read_b128 v[12:15], v25 offset:43008
	v_fmac_f32_e32 v40, v34, v34
	s_waitcnt lgkmcnt(1)
	v_fmac_f32_e32 v39, v10, v30
	v_fmac_f32_e32 v37, v11, v30
	s_waitcnt lgkmcnt(0)
	v_fmac_f32_e32 v35, v12, v30
	v_fmac_f32_e32 v33, v13, v30
	ds_read_b128 v[10:13], v25 offset:18432
	ds_read_b128 v[42:45], v25 offset:51200
	v_fmac_f32_e32 v31, v14, v30
	v_fmac_f32_e32 v29, v15, v30
	s_waitcnt lgkmcnt(1)
	v_fmac_f32_e32 v39, v12, v32
	v_fmac_f32_e32 v37, v13, v32
	s_waitcnt lgkmcnt(0)
	v_fmac_f32_e32 v35, v42, v32
	v_fmac_f32_e32 v33, v43, v32
	v_fmac_f32_e32 v31, v44, v32
	v_fmac_f32_e32 v29, v45, v32
	ds_read_b128 v[12:15], v25 offset:26624
	ds_read_b128 v[42:45], v25 offset:59392
	s_waitcnt lgkmcnt(1)
	v_fmac_f32_e32 v39, v14, v34
	v_fmac_f32_e32 v37, v15, v34
	s_waitcnt lgkmcnt(0)
	v_fmac_f32_e32 v35, v42, v34
	v_fmac_f32_e32 v33, v43, v34
	v_fmac_f32_e32 v31, v44, v34
	v_fmac_f32_e32 v29, v45, v34
	ds_read_b128 v[42:45], v25 offset:3072
	ds_read_b128 v[46:49], v25 offset:35840
	s_waitcnt vmcnt(4)
	v_mov_b32_e32 v14, v66
	v_mov_b32_e32 v15, v67
	v_lshlrev_b32_e32 v36, 16, v14
	s_waitcnt lgkmcnt(1)
	v_fmac_f32_e32 v39, v44, v36
	v_fmac_f32_e32 v37, v45, v36
	s_waitcnt lgkmcnt(0)
	v_fmac_f32_e32 v35, v46, v36
	v_fmac_f32_e32 v33, v47, v36
	v_fmac_f32_e32 v31, v48, v36
	v_fmac_f32_e32 v29, v49, v36
	ds_read_b128 v[44:47], v25 offset:11264
	ds_read_b128 v[48:51], v25 offset:44032
	v_and_b32_e32 v14, 0xffff0000, v14
	v_lshlrev_b32_e32 v38, 16, v15
	v_and_b32_e32 v56, 0xffff0000, v15
	s_waitcnt lgkmcnt(1)
	v_fmac_f32_e32 v39, v46, v14
	v_fmac_f32_e32 v37, v47, v14
	s_waitcnt lgkmcnt(0)
	v_fmac_f32_e32 v35, v48, v14
	v_fmac_f32_e32 v33, v49, v14
	v_fmac_f32_e32 v31, v50, v14
	v_fmac_f32_e32 v29, v51, v14
	ds_read_b128 v[46:49], v25 offset:19456
	ds_read_b128 v[50:53], v25 offset:52224
	v_fmac_f32_e32 v40, v36, v36
	v_fmac_f32_e32 v40, v14, v14
	v_fmac_f32_e32 v40, v38, v38
	s_waitcnt lgkmcnt(1)
	v_fmac_f32_e32 v39, v48, v38
	s_waitcnt lgkmcnt(0)
	v_fmac_f32_e32 v29, v53, v38
	v_fmac_f32_e32 v31, v52, v38
	v_pk_fma_f32 v[0:1], v[6:7], v[28:29], v[0:1] op_sel_hi:[1,0,1]
	v_fmac_f32_e32 v33, v51, v38
	v_pk_fma_f32 v[0:1], v[8:9], v[30:31], v[0:1] op_sel_hi:[1,0,1]
	v_fmac_f32_e32 v35, v50, v38
	v_pk_fma_f32 v[0:1], v[10:11], v[32:33], v[0:1] op_sel_hi:[1,0,1]
	v_fmac_f32_e32 v37, v49, v38
	ds_read_b128 v[48:51], v25 offset:27648
	ds_read_b128 v[52:55], v25 offset:60416
	v_pk_fma_f32 v[0:1], v[12:13], v[34:35], v[0:1] op_sel_hi:[1,0,1]
	v_fmac_f32_e32 v40, v56, v56
	v_pk_fma_f32 v[0:1], v[42:43], v[36:37], v[0:1] op_sel_hi:[1,0,1]
	s_waitcnt lgkmcnt(1)
	v_fmac_f32_e32 v37, v51, v56
	v_pk_fma_f32 v[0:1], v[44:45], v[14:15], v[0:1] op_sel_hi:[1,0,1]
	s_waitcnt lgkmcnt(0)
	v_fmac_f32_e32 v35, v52, v56
	v_pk_fma_f32 v[0:1], v[46:47], v[38:39], v[0:1] op_sel_hi:[1,0,1]
	v_fmac_f32_e32 v39, v50, v56
	v_pk_fma_f32 v[22:23], v[48:49], v[56:57], v[0:1] op_sel_hi:[1,0,1]
	v_fmac_f32_e32 v33, v53, v56
	v_fmac_f32_e32 v31, v54, v56
	v_fmac_f32_e32 v29, v55, v56
	s_waitcnt vmcnt(3)
	v_mov_b32_e32 v0, v68
	v_mov_b32_e32 v1, v69
	v_lshlrev_b32_e32 v24, 16, v0
	v_and_b32_e32 v26, 0xffff0000, v0
	v_lshlrev_b32_e32 v28, 16, v1
	v_and_b32_e32 v30, 0xffff0000, v1
	ds_read_b128 v[0:3], v25 offset:4096
	ds_read_b128 v[4:7], v25 offset:36864
	v_fmac_f32_e32 v40, v24, v24
	v_fmac_f32_e32 v40, v26, v26
	v_fmac_f32_e32 v40, v28, v28
	s_waitcnt lgkmcnt(1)
	v_fmac_f32_e32 v39, v2, v24
	v_fmac_f32_e32 v37, v3, v24
	s_waitcnt lgkmcnt(0)
	v_fmac_f32_e32 v35, v4, v24
	v_fmac_f32_e32 v33, v5, v24
	v_fmac_f32_e32 v31, v6, v24
	v_fmac_f32_e32 v29, v7, v24
	ds_read_b128 v[2:5], v25 offset:12288
	ds_read_b128 v[6:9], v25 offset:45056
	v_pk_fma_f32 v[0:1], v[0:1], v[24:25], v[22:23] op_sel_hi:[1,0,1]
	v_fmac_f32_e32 v40, v30, v30
	s_waitcnt lgkmcnt(1)
	v_fmac_f32_e32 v39, v4, v26
	v_fmac_f32_e32 v37, v5, v26
	s_waitcnt lgkmcnt(0)
	v_fmac_f32_e32 v35, v6, v26
	v_fmac_f32_e32 v33, v7, v26
	v_fmac_f32_e32 v31, v8, v26
	v_fmac_f32_e32 v29, v9, v26
	ds_read_b128 v[4:7], v25 offset:20480
	ds_read_b128 v[8:11], v25 offset:53248
	v_pk_fma_f32 v[0:1], v[2:3], v[26:27], v[0:1] op_sel_hi:[1,0,1]
	s_waitcnt lgkmcnt(1)
	v_fmac_f32_e32 v39, v6, v28
	v_fmac_f32_e32 v37, v7, v28
	s_waitcnt lgkmcnt(0)
	v_fmac_f32_e32 v35, v8, v28
	v_fmac_f32_e32 v33, v9, v28
	v_fmac_f32_e32 v31, v10, v28
	v_fmac_f32_e32 v29, v11, v28
	ds_read_b128 v[6:9], v25 offset:28672
	ds_read_b128 v[10:13], v25 offset:61440
	s_waitcnt lgkmcnt(1)
	v_fmac_f32_e32 v39, v8, v30
	v_fmac_f32_e32 v37, v9, v30
	s_waitcnt lgkmcnt(0)
	v_fmac_f32_e32 v35, v10, v30
	v_fmac_f32_e32 v33, v11, v30
	v_fmac_f32_e32 v31, v12, v30
	v_fmac_f32_e32 v29, v13, v30
	s_waitcnt vmcnt(2)
	v_mov_b32_e32 v8, v70
	v_mov_b32_e32 v9, v71
	v_lshlrev_b32_e32 v32, 16, v8
	v_and_b32_e32 v34, 0xffff0000, v8
	v_lshlrev_b32_e32 v36, 16, v9
	v_and_b32_e32 v38, 0xffff0000, v9
	ds_read_b128 v[8:11], v25 offset:5120
	ds_read_b128 v[12:15], v25 offset:37888
	v_fmac_f32_e32 v40, v32, v32
	v_fmac_f32_e32 v40, v34, v34
	v_fmac_f32_e32 v40, v36, v36
	s_waitcnt lgkmcnt(1)
	v_fmac_f32_e32 v39, v10, v32
	v_fmac_f32_e32 v37, v11, v32
	s_waitcnt lgkmcnt(0)
	v_fmac_f32_e32 v35, v12, v32
	v_fmac_f32_e32 v33, v13, v32
	v_fmac_f32_e32 v31, v14, v32
	v_fmac_f32_e32 v29, v15, v32
	ds_read_b128 v[10:13], v25 offset:13312
	ds_read_b128 v[14:17], v25 offset:46080
	v_fmac_f32_e32 v40, v38, v38
	s_waitcnt lgkmcnt(1)
	v_fmac_f32_e32 v39, v12, v34
	v_fmac_f32_e32 v37, v13, v34
	s_waitcnt lgkmcnt(0)
	v_fmac_f32_e32 v35, v14, v34
	v_fmac_f32_e32 v33, v15, v34
	ds_read_b128 v[12:15], v25 offset:21504
	ds_read_b128 v[42:45], v25 offset:54272
	v_fmac_f32_e32 v31, v16, v34
	v_fmac_f32_e32 v29, v17, v34
	s_waitcnt lgkmcnt(1)
	v_fmac_f32_e32 v39, v14, v36
	v_fmac_f32_e32 v37, v15, v36
	s_waitcnt lgkmcnt(0)
	v_fmac_f32_e32 v35, v42, v36
	v_fmac_f32_e32 v33, v43, v36
	v_fmac_f32_e32 v31, v44, v36
	v_fmac_f32_e32 v29, v45, v36
	ds_read_b128 v[14:17], v25 offset:29696
	ds_read_b128 v[42:45], v25 offset:62464
	s_waitcnt lgkmcnt(1)
	v_fmac_f32_e32 v39, v16, v38
	v_fmac_f32_e32 v37, v17, v38
	s_waitcnt lgkmcnt(0)
	v_fmac_f32_e32 v35, v42, v38
	v_fmac_f32_e32 v33, v43, v38
	v_fmac_f32_e32 v31, v44, v38
	v_fmac_f32_e32 v29, v45, v38
	ds_read_b128 v[42:45], v25 offset:6144
	ds_read_b128 v[46:49], v25 offset:38912
	s_waitcnt vmcnt(1)
	v_mov_b32_e32 v16, v72
	v_mov_b32_e32 v17, v73
	v_lshlrev_b32_e32 v54, 16, v16
	s_waitcnt lgkmcnt(1)
	v_fmac_f32_e32 v39, v44, v54
	v_fmac_f32_e32 v37, v45, v54
	s_waitcnt lgkmcnt(0)
	v_fmac_f32_e32 v35, v46, v54
	v_fmac_f32_e32 v33, v47, v54
	v_fmac_f32_e32 v31, v48, v54
	v_fmac_f32_e32 v29, v49, v54
	ds_read_b128 v[44:47], v25 offset:14336
	ds_read_b128 v[48:51], v25 offset:47104
	v_and_b32_e32 v56, 0xffff0000, v16
	v_lshlrev_b32_e32 v58, 16, v17
	v_and_b32_e32 v16, 0xffff0000, v17
	s_waitcnt lgkmcnt(1)
	v_fmac_f32_e32 v37, v47, v56
	s_waitcnt lgkmcnt(0)
	v_fmac_f32_e32 v29, v51, v56
	v_fmac_f32_e32 v31, v50, v56
	v_pk_fma_f32 v[0:1], v[4:5], v[28:29], v[0:1] op_sel_hi:[1,0,1]
	v_fmac_f32_e32 v33, v49, v56
	v_pk_fma_f32 v[0:1], v[6:7], v[30:31], v[0:1] op_sel_hi:[1,0,1]
	v_fmac_f32_e32 v35, v48, v56
	v_pk_fma_f32 v[0:1], v[8:9], v[32:33], v[0:1] op_sel_hi:[1,0,1]
	v_fmac_f32_e32 v39, v46, v56
	v_pk_fma_f32 v[0:1], v[10:11], v[34:35], v[0:1] op_sel_hi:[1,0,1]
	ds_read_b128 v[46:49], v25 offset:22528
	ds_read_b128 v[50:53], v25 offset:55296
	v_pk_fma_f32 v[0:1], v[12:13], v[36:37], v[0:1] op_sel_hi:[1,0,1]
	v_fmac_f32_e32 v40, v54, v54
	v_pk_fma_f32 v[0:1], v[14:15], v[38:39], v[0:1] op_sel_hi:[1,0,1]
	s_waitcnt lgkmcnt(1)
	v_fmac_f32_e32 v39, v48, v58
	v_pk_fma_f32 v[0:1], v[42:43], v[54:55], v[0:1] op_sel_hi:[1,0,1]
	v_fmac_f32_e32 v37, v49, v58
	v_pk_fma_f32 v[0:1], v[44:45], v[56:57], v[0:1] op_sel_hi:[1,0,1]
	s_waitcnt lgkmcnt(0)
	v_fmac_f32_e32 v35, v50, v58
	v_pk_fma_f32 v[12:13], v[46:47], v[58:59], v[0:1] op_sel_hi:[1,0,1]
	ds_read_b128 v[0:3], v25 offset:30720
	ds_read_b128 v[4:7], v25 offset:63488
	v_fmac_f32_e32 v33, v51, v58
	v_fmac_f32_e32 v31, v52, v58
	v_fmac_f32_e32 v29, v53, v58
	s_waitcnt lgkmcnt(1)
	v_fmac_f32_e32 v39, v2, v16
	v_fmac_f32_e32 v37, v3, v16
	s_waitcnt lgkmcnt(0)
	v_fmac_f32_e32 v35, v4, v16
	v_fmac_f32_e32 v33, v5, v16
	v_fmac_f32_e32 v31, v6, v16
	v_fmac_f32_e32 v29, v7, v16
	v_fmac_f32_e32 v40, v56, v56
	v_fmac_f32_e32 v40, v58, v58
	v_fmac_f32_e32 v40, v16, v16
	s_waitcnt vmcnt(0)
	v_mov_b32_e32 v2, v74
	v_mov_b32_e32 v3, v75
	v_lshlrev_b32_e32 v24, 16, v2
	v_and_b32_e32 v22, 0xffff0000, v2
	v_lshlrev_b32_e32 v20, 16, v3
	v_and_b32_e32 v14, 0xffff0000, v3
	ds_read_b128 v[2:5], v25 offset:7168
	ds_read_b128 v[6:9], v25 offset:39936
	v_fmac_f32_e32 v40, v24, v24
	v_fmac_f32_e32 v40, v22, v22
	v_fmac_f32_e32 v40, v20, v20
	s_waitcnt lgkmcnt(1)
	v_fmac_f32_e32 v39, v4, v24
	v_fmac_f32_e32 v37, v5, v24
	s_waitcnt lgkmcnt(0)
	v_fmac_f32_e32 v35, v6, v24
	v_fmac_f32_e32 v33, v7, v24
	v_fmac_f32_e32 v31, v8, v24
	v_fmac_f32_e32 v29, v9, v24
	ds_read_b128 v[4:7], v25 offset:15360
	ds_read_b128 v[8:11], v25 offset:48128
	v_fmac_f32_e32 v40, v14, v14
	s_waitcnt lgkmcnt(1)
	v_fmac_f32_e32 v39, v6, v22
	v_fmac_f32_e32 v37, v7, v22
	s_waitcnt lgkmcnt(0)
	v_fmac_f32_e32 v35, v8, v22
	v_fmac_f32_e32 v33, v9, v22
	ds_read_b128 v[6:9], v25 offset:23552
	ds_read_b128 v[42:45], v25 offset:56320
	v_fmac_f32_e32 v31, v10, v22
	v_fmac_f32_e32 v29, v11, v22
	s_waitcnt lgkmcnt(1)
	v_fmac_f32_e32 v39, v8, v20
	v_fmac_f32_e32 v37, v9, v20
	s_waitcnt lgkmcnt(0)
	v_fmac_f32_e32 v35, v42, v20
	v_fmac_f32_e32 v33, v43, v20
	v_fmac_f32_e32 v31, v44, v20
	v_fmac_f32_e32 v29, v45, v20
	ds_read_b128 v[8:11], v25 offset:31744
	ds_read_b128 v[42:45], v25 offset:64512
	s_waitcnt lgkmcnt(1)
	v_fmac_f32_e32 v39, v10, v14
	v_mbcnt_lo_u32_b32 v10, -1, 0
	v_mbcnt_hi_u32_b32 v10, -1, v10
	v_fmac_f32_e32 v37, v11, v14
	v_lshlrev_b32_e32 v10, 2, v10
	v_xor_b32_e32 v10, 4, v10
	ds_bpermute_b32 v10, v10, v40
	v_mbcnt_lo_u32_b32 v11, -1, 0
	v_mbcnt_hi_u32_b32 v11, -1, v11
	s_waitcnt lgkmcnt(1)
	v_fmac_f32_e32 v35, v42, v14
	v_lshlrev_b32_e32 v11, 2, v11
	v_xor_b32_e32 v11, 8, v11
	s_waitcnt lgkmcnt(0)
	v_add_f32_e32 v10, v40, v10
	ds_bpermute_b32 v11, v11, v10
	v_fmac_f32_e32 v33, v43, v14
	v_fmac_f32_e32 v31, v44, v14
	v_fmac_f32_e32 v29, v45, v14
	s_waitcnt lgkmcnt(0)
	v_add_f32_e32 v10, v10, v11
	v_mbcnt_lo_u32_b32 v11, -1, 0
	v_mbcnt_hi_u32_b32 v11, -1, v11
	s_nop 0
	v_lshlrev_b32_e32 v11, 2, v11
	v_xor_b32_e32 v11, 16, v11
	ds_bpermute_b32 v11, v11, v10
	s_waitcnt lgkmcnt(0)
	v_add_f32_e32 v10, v10, v11
	v_mbcnt_lo_u32_b32 v11, -1, 0
	v_mbcnt_hi_u32_b32 v11, -1, v11
	s_nop 0
	v_lshlrev_b32_e32 v11, 2, v11
	v_xor_b32_e32 v11, 32, v11
	ds_bpermute_b32 v11, v11, v10
	s_waitcnt lgkmcnt(0)
	v_add_f32_e32 v10, v10, v11
	v_mbcnt_lo_u32_b32 v11, -1, 0
	v_mbcnt_hi_u32_b32 v11, -1, v11
	s_nop 0
	v_lshlrev_b32_e32 v11, 2, v11
	v_xor_b32_e32 v11, 64, v11
	ds_bpermute_b32 v11, v11, v10
	s_waitcnt lgkmcnt(0)
	v_add_f32_e32 v10, v10, v11
	v_mbcnt_lo_u32_b32 v11, -1, 0
	v_mbcnt_hi_u32_b32 v11, -1, v11
	v_mbcnt_lo_u32_b32 v15, -1, 0
	v_mbcnt_hi_u32_b32 v15, -1, v15
	v_mbcnt_lo_u32_b32 v17, -1, 0
	v_mbcnt_hi_u32_b32 v17, -1, v17
	v_mbcnt_lo_u32_b32 v21, -1, 0
	v_mbcnt_hi_u32_b32 v21, -1, v21
	v_mbcnt_lo_u32_b32 v23, -1, 0
	v_mbcnt_hi_u32_b32 v23, -1, v23
	v_mbcnt_lo_u32_b32 v26, -1, 0
	v_mbcnt_hi_u32_b32 v26, -1, v26
	v_mbcnt_lo_u32_b32 v27, -1, 0
	v_mbcnt_hi_u32_b32 v27, -1, v27
	s_nop 0
	v_lshlrev_b32_e32 v15, 2, v15
	v_lshlrev_b32_e32 v17, 2, v17
	v_xor_b32_e32 v17, 8, v17
	v_lshlrev_b32_e32 v23, 2, v23
	v_pk_fma_f32 v[0:1], v[0:1], v[16:17], v[12:13] op_sel_hi:[1,0,1]
	v_lshlrev_b32_e32 v21, 2, v21
	v_xor_b32_e32 v23, 32, v23
	v_pk_fma_f32 v[0:1], v[2:3], v[24:25], v[0:1] op_sel_hi:[1,0,1]
	v_xor_b32_e32 v21, 16, v21
	v_mbcnt_lo_u32_b32 v28, -1, 0
	v_mbcnt_hi_u32_b32 v28, -1, v28
	v_pk_fma_f32 v[0:1], v[4:5], v[22:23], v[0:1] op_sel_hi:[1,0,1]
	v_xor_b32_e32 v15, 4, v15
	v_lshlrev_b32_e32 v28, 2, v28
	v_pk_fma_f32 v[0:1], v[6:7], v[20:21], v[0:1] op_sel_hi:[1,0,1]
	v_xor_b32_e32 v28, 4, v28
	v_pk_fma_f32 v[0:1], v[8:9], v[14:15], v[0:1] op_sel_hi:[1,0,1]
	ds_bpermute_b32 v2, v15, v0
	ds_bpermute_b32 v3, v28, v1
	v_mbcnt_lo_u32_b32 v30, -1, 0
	v_mbcnt_hi_u32_b32 v30, -1, v30
	v_mbcnt_lo_u32_b32 v32, -1, 0
	v_mbcnt_hi_u32_b32 v32, -1, v32
	v_mbcnt_lo_u32_b32 v34, -1, 0
	v_mbcnt_hi_u32_b32 v34, -1, v34
	v_mbcnt_lo_u32_b32 v36, -1, 0
	v_mbcnt_hi_u32_b32 v36, -1, v36
	s_waitcnt lgkmcnt(0)
	v_pk_add_f32 v[0:1], v[0:1], v[2:3]
	v_lshlrev_b32_e32 v30, 2, v30
	v_xor_b32_e32 v30, 8, v30
	ds_bpermute_b32 v2, v17, v0
	ds_bpermute_b32 v3, v30, v1
	v_lshlrev_b32_e32 v32, 2, v32
	v_xor_b32_e32 v32, 16, v32
	v_lshlrev_b32_e32 v34, 2, v34
	v_xor_b32_e32 v34, 32, v34
	s_waitcnt lgkmcnt(0)
	v_pk_add_f32 v[0:1], v[0:1], v[2:3]
	ds_bpermute_b32 v2, v21, v0
	ds_bpermute_b32 v3, v32, v1
	v_lshlrev_b32_e32 v26, 2, v26
	v_lshlrev_b32_e32 v36, 2, v36
	v_xor_b32_e32 v26, 64, v26
	v_xor_b32_e32 v36, 64, v36
	s_waitcnt lgkmcnt(0)
	v_pk_add_f32 v[0:1], v[0:1], v[2:3]
	ds_bpermute_b32 v2, v23, v0
	ds_bpermute_b32 v3, v34, v1
	v_lshlrev_b32_e32 v11, 2, v11
	v_lshlrev_b32_e32 v27, 2, v27
	v_xor_b32_e32 v11, 0x80, v11
	v_xor_b32_e32 v27, 0x80, v27
	s_waitcnt lgkmcnt(0)
	v_pk_add_f32 v[0:1], v[0:1], v[2:3]
	ds_bpermute_b32 v2, v26, v0
	ds_bpermute_b32 v3, v36, v1
	ds_bpermute_b32 v11, v11, v10
	s_waitcnt lgkmcnt(1)
	v_pk_add_f32 v[0:1], v[0:1], v[2:3]
	v_mbcnt_lo_u32_b32 v3, -1, 0
	v_mbcnt_hi_u32_b32 v3, -1, v3
	v_mbcnt_lo_u32_b32 v4, -1, 0
	v_mbcnt_hi_u32_b32 v4, -1, v4
	v_mbcnt_lo_u32_b32 v5, -1, 0
	v_mbcnt_hi_u32_b32 v5, -1, v5
	ds_bpermute_b32 v2, v27, v0
	v_lshlrev_b32_e32 v4, 2, v4
	v_xor_b32_e32 v4, 4, v4
	ds_bpermute_b32 v4, v4, v39
	v_lshlrev_b32_e32 v5, 2, v5
	v_xor_b32_e32 v5, 8, v5
	v_lshlrev_b32_e32 v3, 2, v3
	v_xor_b32_e32 v3, 0x80, v3
	s_waitcnt lgkmcnt(0)
	v_add_f32_e32 v4, v39, v4
	ds_bpermute_b32 v5, v5, v4
	ds_bpermute_b32 v3, v3, v1
	s_waitcnt lgkmcnt(1)
	v_add_f32_e32 v4, v4, v5
	v_mbcnt_lo_u32_b32 v5, -1, 0
	v_mbcnt_hi_u32_b32 v5, -1, v5
	s_nop 0
	v_lshlrev_b32_e32 v5, 2, v5
	v_xor_b32_e32 v5, 16, v5
	ds_bpermute_b32 v5, v5, v4
	s_waitcnt lgkmcnt(0)
	v_add_f32_e32 v4, v4, v5
	v_mbcnt_lo_u32_b32 v5, -1, 0
	v_mbcnt_hi_u32_b32 v5, -1, v5
	s_nop 0
	v_lshlrev_b32_e32 v5, 2, v5
	v_xor_b32_e32 v5, 32, v5
	ds_bpermute_b32 v5, v5, v4
	s_waitcnt lgkmcnt(0)
	v_add_f32_e32 v4, v4, v5
	v_mbcnt_lo_u32_b32 v5, -1, 0
	v_mbcnt_hi_u32_b32 v5, -1, v5
	s_nop 0
	v_lshlrev_b32_e32 v5, 2, v5
	v_xor_b32_e32 v5, 64, v5
	ds_bpermute_b32 v5, v5, v4
	s_waitcnt lgkmcnt(0)
	v_add_f32_e32 v5, v4, v5
	v_mbcnt_lo_u32_b32 v4, -1, 0
	v_mbcnt_hi_u32_b32 v4, -1, v4
	s_nop 0
	v_lshlrev_b32_e32 v4, 2, v4
	v_xor_b32_e32 v4, 0x80, v4
	ds_bpermute_b32 v6, v4, v5
	v_mbcnt_lo_u32_b32 v4, -1, 0
	v_mbcnt_hi_u32_b32 v4, -1, v4
	v_mbcnt_lo_u32_b32 v7, -1, 0
	v_mbcnt_hi_u32_b32 v7, -1, v7
	s_nop 0
	v_lshlrev_b32_e32 v4, 2, v4
	v_xor_b32_e32 v4, 4, v4
	ds_bpermute_b32 v4, v4, v37
	v_lshlrev_b32_e32 v7, 2, v7
	v_xor_b32_e32 v7, 8, v7
	s_waitcnt lgkmcnt(0)
	v_add_f32_e32 v4, v37, v4
	ds_bpermute_b32 v7, v7, v4
	s_waitcnt lgkmcnt(0)
	v_add_f32_e32 v4, v4, v7
	v_mbcnt_lo_u32_b32 v7, -1, 0
	v_mbcnt_hi_u32_b32 v7, -1, v7
	s_nop 0
	v_lshlrev_b32_e32 v7, 2, v7
	v_xor_b32_e32 v7, 16, v7
	ds_bpermute_b32 v7, v7, v4
	s_waitcnt lgkmcnt(0)
	v_add_f32_e32 v4, v4, v7
	v_mbcnt_lo_u32_b32 v7, -1, 0
	v_mbcnt_hi_u32_b32 v7, -1, v7
	s_nop 0
	v_lshlrev_b32_e32 v7, 2, v7
	v_xor_b32_e32 v7, 32, v7
	ds_bpermute_b32 v7, v7, v4
	s_waitcnt lgkmcnt(0)
	v_add_f32_e32 v4, v4, v7
	v_mbcnt_lo_u32_b32 v7, -1, 0
	v_mbcnt_hi_u32_b32 v7, -1, v7
	s_nop 0
	v_lshlrev_b32_e32 v7, 2, v7
	v_xor_b32_e32 v7, 64, v7
	ds_bpermute_b32 v7, v7, v4
	s_waitcnt lgkmcnt(0)
	v_add_f32_e32 v7, v4, v7
	v_mbcnt_lo_u32_b32 v4, -1, 0
	v_mbcnt_hi_u32_b32 v4, -1, v4
	s_nop 0
	v_lshlrev_b32_e32 v4, 2, v4
	v_xor_b32_e32 v4, 0x80, v4
	ds_bpermute_b32 v8, v4, v7
	v_mbcnt_lo_u32_b32 v4, -1, 0
	v_mbcnt_hi_u32_b32 v4, -1, v4
	v_mbcnt_lo_u32_b32 v9, -1, 0
	v_mbcnt_hi_u32_b32 v9, -1, v9
	s_nop 0
	v_lshlrev_b32_e32 v4, 2, v4
	v_xor_b32_e32 v4, 4, v4
	ds_bpermute_b32 v4, v4, v35
	v_lshlrev_b32_e32 v9, 2, v9
	v_xor_b32_e32 v9, 8, v9
	s_waitcnt lgkmcnt(0)
	v_add_f32_e32 v4, v35, v4
	ds_bpermute_b32 v9, v9, v4
	s_waitcnt lgkmcnt(0)
	v_add_f32_e32 v4, v4, v9
	v_mbcnt_lo_u32_b32 v9, -1, 0
	v_mbcnt_hi_u32_b32 v9, -1, v9
	s_nop 0
	v_lshlrev_b32_e32 v9, 2, v9
	v_xor_b32_e32 v9, 16, v9
	ds_bpermute_b32 v9, v9, v4
	s_waitcnt lgkmcnt(0)
	v_add_f32_e32 v4, v4, v9
	v_mbcnt_lo_u32_b32 v9, -1, 0
	v_mbcnt_hi_u32_b32 v9, -1, v9
	s_nop 0
	v_lshlrev_b32_e32 v9, 2, v9
	v_xor_b32_e32 v9, 32, v9
	ds_bpermute_b32 v9, v9, v4
	s_waitcnt lgkmcnt(0)
	v_add_f32_e32 v4, v4, v9
	v_mbcnt_lo_u32_b32 v9, -1, 0
	v_mbcnt_hi_u32_b32 v9, -1, v9
	s_nop 0
	v_lshlrev_b32_e32 v9, 2, v9
	v_xor_b32_e32 v9, 64, v9
	ds_bpermute_b32 v9, v9, v4
	s_waitcnt lgkmcnt(0)
	v_add_f32_e32 v9, v4, v9
	v_mbcnt_lo_u32_b32 v4, -1, 0
	v_mbcnt_hi_u32_b32 v4, -1, v4
	s_nop 0
	v_lshlrev_b32_e32 v4, 2, v4
	v_xor_b32_e32 v4, 0x80, v4
	ds_bpermute_b32 v12, v4, v9
	v_mbcnt_lo_u32_b32 v4, -1, 0
	v_mbcnt_hi_u32_b32 v4, -1, v4
	v_mbcnt_lo_u32_b32 v13, -1, 0
	v_mbcnt_hi_u32_b32 v13, -1, v13
	s_nop 0
	v_lshlrev_b32_e32 v4, 2, v4
	v_xor_b32_e32 v4, 4, v4
	ds_bpermute_b32 v4, v4, v33
	v_lshlrev_b32_e32 v13, 2, v13
	v_xor_b32_e32 v13, 8, v13
	s_waitcnt lgkmcnt(0)
	v_add_f32_e32 v4, v33, v4
	ds_bpermute_b32 v13, v13, v4
	s_waitcnt lgkmcnt(0)
	v_add_f32_e32 v4, v4, v13
	v_mbcnt_lo_u32_b32 v13, -1, 0
	v_mbcnt_hi_u32_b32 v13, -1, v13
	s_nop 0
	v_lshlrev_b32_e32 v13, 2, v13
	v_xor_b32_e32 v13, 16, v13
	ds_bpermute_b32 v13, v13, v4
	s_waitcnt lgkmcnt(0)
	v_add_f32_e32 v4, v4, v13
	v_mbcnt_lo_u32_b32 v13, -1, 0
	v_mbcnt_hi_u32_b32 v13, -1, v13
	s_nop 0
	v_lshlrev_b32_e32 v13, 2, v13
	v_xor_b32_e32 v13, 32, v13
	ds_bpermute_b32 v13, v13, v4
	s_waitcnt lgkmcnt(0)
	v_add_f32_e32 v4, v4, v13
	v_mbcnt_lo_u32_b32 v13, -1, 0
	v_mbcnt_hi_u32_b32 v13, -1, v13
	s_nop 0
	v_lshlrev_b32_e32 v13, 2, v13
	v_xor_b32_e32 v13, 64, v13
	ds_bpermute_b32 v13, v13, v4
	s_waitcnt lgkmcnt(0)
	v_add_f32_e32 v13, v4, v13
	v_mbcnt_lo_u32_b32 v4, -1, 0
	v_mbcnt_hi_u32_b32 v4, -1, v4
	s_nop 0
	v_lshlrev_b32_e32 v4, 2, v4
	v_xor_b32_e32 v4, 0x80, v4
	ds_bpermute_b32 v14, v4, v13
	v_mbcnt_lo_u32_b32 v4, -1, 0
	v_mbcnt_hi_u32_b32 v4, -1, v4
	v_mbcnt_lo_u32_b32 v15, -1, 0
	v_mbcnt_hi_u32_b32 v15, -1, v15
	s_nop 0
	v_lshlrev_b32_e32 v4, 2, v4
	v_xor_b32_e32 v4, 4, v4
	ds_bpermute_b32 v4, v4, v31
	v_lshlrev_b32_e32 v15, 2, v15
	v_xor_b32_e32 v15, 8, v15
	s_waitcnt lgkmcnt(0)
	v_add_f32_e32 v4, v31, v4
	ds_bpermute_b32 v15, v15, v4
	s_waitcnt lgkmcnt(0)
	v_add_f32_e32 v4, v4, v15
	v_mbcnt_lo_u32_b32 v15, -1, 0
	v_mbcnt_hi_u32_b32 v15, -1, v15
	s_nop 0
	v_lshlrev_b32_e32 v15, 2, v15
	v_xor_b32_e32 v15, 16, v15
	ds_bpermute_b32 v15, v15, v4
	s_waitcnt lgkmcnt(0)
	v_add_f32_e32 v4, v4, v15
	v_mbcnt_lo_u32_b32 v15, -1, 0
	v_mbcnt_hi_u32_b32 v15, -1, v15
	s_nop 0
	v_lshlrev_b32_e32 v15, 2, v15
	v_xor_b32_e32 v15, 32, v15
	ds_bpermute_b32 v15, v15, v4
	s_waitcnt lgkmcnt(0)
	v_add_f32_e32 v4, v4, v15
	v_mbcnt_lo_u32_b32 v15, -1, 0
	v_mbcnt_hi_u32_b32 v15, -1, v15
	s_nop 0
	v_lshlrev_b32_e32 v15, 2, v15
	v_xor_b32_e32 v15, 64, v15
	ds_bpermute_b32 v15, v15, v4
	s_waitcnt lgkmcnt(0)
	v_add_f32_e32 v15, v4, v15
	v_mbcnt_lo_u32_b32 v4, -1, 0
	v_mbcnt_hi_u32_b32 v4, -1, v4
	s_nop 0
	v_lshlrev_b32_e32 v4, 2, v4
	v_xor_b32_e32 v4, 0x80, v4
	ds_bpermute_b32 v16, v4, v15
	v_mbcnt_lo_u32_b32 v4, -1, 0
	v_mbcnt_hi_u32_b32 v4, -1, v4
	v_mbcnt_lo_u32_b32 v17, -1, 0
	v_mbcnt_hi_u32_b32 v17, -1, v17
	s_nop 0
	v_lshlrev_b32_e32 v4, 2, v4
	v_xor_b32_e32 v4, 4, v4
	ds_bpermute_b32 v4, v4, v29
	v_lshlrev_b32_e32 v17, 2, v17
	v_xor_b32_e32 v17, 8, v17
	s_waitcnt lgkmcnt(0)
	v_add_f32_e32 v4, v29, v4
	ds_bpermute_b32 v17, v17, v4
	s_waitcnt lgkmcnt(0)
	v_add_f32_e32 v4, v4, v17
	v_mbcnt_lo_u32_b32 v17, -1, 0
	v_mbcnt_hi_u32_b32 v17, -1, v17
	s_nop 0
	v_lshlrev_b32_e32 v17, 2, v17
	v_xor_b32_e32 v17, 16, v17
	ds_bpermute_b32 v17, v17, v4
	s_waitcnt lgkmcnt(0)
	v_add_f32_e32 v4, v4, v17
	v_mbcnt_lo_u32_b32 v17, -1, 0
	v_mbcnt_hi_u32_b32 v17, -1, v17
	s_nop 0
	v_lshlrev_b32_e32 v17, 2, v17
	v_xor_b32_e32 v17, 32, v17
	ds_bpermute_b32 v17, v17, v4
	s_waitcnt lgkmcnt(0)
	v_add_f32_e32 v4, v4, v17
	v_mbcnt_lo_u32_b32 v17, -1, 0
	v_mbcnt_hi_u32_b32 v17, -1, v17
	s_nop 0
	v_lshlrev_b32_e32 v17, 2, v17
	v_xor_b32_e32 v17, 64, v17
	ds_bpermute_b32 v17, v17, v4
	s_waitcnt lgkmcnt(0)
	v_add_f32_e32 v17, v4, v17
	v_mbcnt_lo_u32_b32 v4, -1, 0
	v_mbcnt_hi_u32_b32 v4, -1, v4
	s_nop 0
	v_lshlrev_b32_e32 v4, 2, v4
	v_xor_b32_e32 v4, 0x80, v4
	ds_bpermute_b32 v20, v4, v17
	s_and_saveexec_b64 s[0:1], s[36:37]
	s_cbranch_execz .LBB0_1621
	v_add_f32_e32 v4, v10, v11
	v_fmamk_f32 v4, v4, 0x3a000000, v253
	s_mov_b32 s13, 0xf800000
	v_cmp_gt_f32_e32 vcc, s13, v4
	v_mul_f32_e32 v10, 0x4f800000, v4
	v_add_f32_e32 v5, v5, v6
	v_cndmask_b32_e32 v4, v4, v10, vcc
	v_sqrt_f32_e32 v10, v4
	v_pk_add_f32 v[0:1], v[0:1], v[2:3]
	v_add_f32_e32 v7, v7, v8
	v_add_f32_e32 v9, v9, v12
	v_add_u32_e32 v11, -1, v10
	v_fma_f32 v21, -v11, v10, v4
	v_cmp_ge_f32_e64 s[38:39], 0, v21
	v_add_u32_e32 v21, 1, v10
	v_add_f32_e32 v13, v13, v14
	v_cndmask_b32_e64 v11, v10, v11, s[38:39]
	v_fma_f32 v10, -v21, v10, v4
	v_cmp_lt_f32_e64 s[38:39], 0, v10
	s_nop 1
	v_cndmask_b32_e64 v10, v11, v21, s[38:39]
	v_mul_f32_e32 v11, 0x37800000, v10
	v_cndmask_b32_e32 v10, v10, v11, vcc
	v_mov_b32_e32 v11, 0x260
	v_cmp_class_f32_e32 vcc, v4, v11
	s_nop 1
	v_cndmask_b32_e32 v4, v10, v4, vcc
	v_div_scale_f32 v10, s[18:19], v4, v4, 1.0
	v_rcp_f32_e32 v11, v10
	s_nop 0
	v_fma_f32 v21, -v10, v11, 1.0
	v_fmac_f32_e32 v11, v21, v11
	v_div_scale_f32 v21, vcc, 1.0, v4, 1.0
	v_mul_f32_e32 v22, v21, v11
	v_fma_f32 v23, -v10, v22, v21
	v_fmac_f32_e32 v22, v23, v11
	v_fma_f32 v10, -v10, v22, v21
	v_div_fmas_f32 v10, v10, v11, v22
	v_div_fixup_f32 v4, v10, v4, 1.0
	v_mul_f32_e32 v5, v4, v5
	v_pk_mul_f32 v[0:1], v[4:5], v[0:1] op_sel_hi:[0,1]
	v_cmp_gt_f32_e32 vcc, v1, v0
	v_mul_f32_e32 v7, v4, v7
	v_mul_f32_e32 v9, v4, v9
	v_cndmask_b32_e32 v2, v0, v1, vcc
	v_cmp_gt_f32_e64 s[38:39], v5, v2
	v_mul_f32_e32 v13, v4, v13
	v_cndmask_b32_e64 v3, 0, 1, vcc
	v_cndmask_b32_e64 v2, v2, v5, s[38:39]
	v_cmp_gt_f32_e64 s[40:41], v7, v2
	v_add_f32_e32 v11, v15, v16
	v_cndmask_b32_e64 v3, v3, 2, s[38:39]
	v_cndmask_b32_e64 v2, v2, v7, s[40:41]
	v_cmp_gt_f32_e64 s[42:43], v9, v2
	v_mul_f32_e32 v11, v4, v11
	v_cndmask_b32_e64 v3, v3, 3, s[40:41]
	v_cndmask_b32_e64 v2, v2, v9, s[42:43]
	v_cmp_gt_f32_e64 s[44:45], v13, v2
	s_waitcnt lgkmcnt(0)
	v_add_f32_e32 v10, v17, v20
	v_cndmask_b32_e64 v3, v3, 4, s[42:43]
	v_cndmask_b32_e64 v2, v2, v13, s[44:45]
	v_cmp_gt_f32_e64 s[46:47], v11, v2
	v_mul_f32_e32 v10, v4, v10
	v_cndmask_b32_e64 v3, v3, 5, s[44:45]
	v_cndmask_b32_e64 v2, v2, v11, s[46:47]
	v_cmp_ngt_f32_e64 s[48:49], v10, v2
	v_cndmask_b32_e64 v3, v3, 6, s[46:47]
	s_and_b64 s[18:19], s[48:49], s[46:47]
	v_cndmask_b32_e64 v176, 7, v3, s[48:49]
	v_cmp_ne_u32_e64 s[46:47], 0, v176
	v_cmp_lt_f32_e64 s[50:51], s11, v0
	s_and_b64 s[46:47], s[46:47], s[50:51]
	v_mov_b32_e32 v3, 0xff61b1e6
	v_cndmask_b32_e64 v0, v3, v0, s[46:47]
	v_cmp_ne_u32_e64 s[44:45], 1, v176
	v_cmp_gt_f32_e64 s[46:47], v1, v0
	s_and_b64 s[44:45], s[44:45], s[46:47]
	v_cndmask_b32_e64 v0, v0, v1, s[44:45]
	v_cmp_ne_u32_e64 s[42:43], 2, v176
	v_cmp_gt_f32_e64 s[46:47], v5, v0
	s_and_b64 s[42:43], s[42:43], s[46:47]
	v_cndmask_b32_e64 v0, v0, v5, s[42:43]
	v_cmp_ne_u32_e64 s[40:41], 3, v176
	v_cmp_gt_f32_e64 s[46:47], v7, v0
	s_and_b64 s[40:41], s[40:41], s[46:47]
	v_cndmask_b32_e64 v0, v0, v7, s[40:41]
	v_cmp_ne_u32_e64 s[38:39], 4, v176
	v_cmp_gt_f32_e64 s[46:47], v9, v0
	s_and_b64 s[38:39], s[38:39], s[46:47]
	v_cndmask_b32_e64 v0, v0, v9, s[38:39]
	v_cmp_ne_u32_e32 vcc, 5, v176
	v_cmp_gt_f32_e64 s[46:47], v13, v0
	s_and_b64 vcc, vcc, s[46:47]
	v_cndmask_b32_e32 v0, v0, v13, vcc
	v_cmp_ngt_f32_e64 s[46:47], v11, v0
	s_or_b64 s[46:47], s[18:19], s[46:47]
	v_cndmask_b32_e64 v2, v10, v2, s[48:49]
	v_cndmask_b32_e64 v1, v11, v0, s[46:47]
	v_cmp_gt_f32_e64 s[50:51], v10, v1
	s_and_b64 s[50:51], s[48:49], s[50:51]
	v_cndmask_b32_e64 v0, 0, 1, s[44:45]
	v_cndmask_b32_e64 v1, v1, v10, s[50:51]
	v_sub_f32_e32 v1, v2, v1
	v_mul_f32_e32 v1, 0x3fb8aa3b, v1
	v_exp_f32_e32 v1, v1
	v_cndmask_b32_e64 v0, v0, 2, s[42:43]
	v_cndmask_b32_e64 v0, v0, 3, s[40:41]
	v_cndmask_b32_e64 v0, v0, 4, s[38:39]
	v_add_f32_e32 v1, 1.0, v1
	v_div_scale_f32 v2, s[18:19], v1, v1, 1.0
	v_rcp_f32_e32 v3, v2
	v_cndmask_b32_e64 v0, v0, 5, vcc
	s_add_u32 s18, s52, s8
	s_addc_u32 s19, s53, s9
	v_fma_f32 v5, -v2, v3, 1.0
	v_fmac_f32_e32 v3, v5, v3
	v_div_scale_f32 v5, vcc, 1.0, v1, 1.0
	v_mul_f32_e32 v6, v5, v3
	v_fma_f32 v7, -v2, v6, v5
	v_fmac_f32_e32 v6, v7, v3
	v_fma_f32 v2, -v2, v6, v5
	v_div_fmas_f32 v2, v2, v3, v6
	v_div_fixup_f32 v5, v2, v1, 1.0
	global_store_dword v177, v4, s[18:19]
	v_mul_u32_u24_e32 v2, 0x2100, v176
	v_mov_b32_e32 v3, v177
	v_lshl_add_u64 v[2:3], v[2:3], 0, s[52:53]
	global_atomic_add v1, v[2:3], v231, off offset:384 sc0
	v_cndmask_b32_e64 v0, 6, v0, s[46:47]
	v_cndmask_b32_e64 v0, v0, 7, s[50:51]
	v_mul_u32_u24_e32 v6, 0x2100, v0
	v_mov_b32_e32 v7, v177
	v_lshl_add_u64 v[6:7], v[6:7], 0, s[52:53]
	global_atomic_add v76, v[6:7], v231, off offset:384 sc0
	v_mov_b32_e32 v11, s56
	s_ashr_i32 s67, s66, 31
	s_lshl_b64 s[18:19], s[66:67], 2
	s_add_u32 s20, s2, s18
	s_addc_u32 s21, s3, s19
	s_add_i32 s22, s66, 1
	s_ashr_i32 s23, s22, 31
	s_add_u32 s18, s4, s18
	v_sub_f32_e32 v10, 1.0, v5
	s_addc_u32 s19, s5, s19
	s_waitcnt vmcnt(1)
	v_lshl_add_u32 v176, v176, 14, v1
	v_lshlrev_b64 v[2:3], 2, v[176:177]
	v_lshl_add_u64 v[6:7], s[68:69], 0, v[2:3]
	v_mov_b32_e32 v1, v177
	global_store_dword v[6:7], v11, off
	v_lshl_add_u64 v[2:3], s[70:71], 0, v[2:3]
	global_store_dword v[2:3], v4, off
	s_waitcnt vmcnt(2)
	v_lshl_add_u32 v0, v0, 14, v76
	v_mov_b32_e32 v1, v177
	v_lshlrev_b64 v[6:7], 2, v[0:1]
	v_lshl_add_u64 v[2:3], s[70:71], 0, v[6:7]
	global_store_dword v[2:3], v4, off
	global_store_dword v177, v10, s[18:19]
	s_lshl_b64 s[18:19], s[22:23], 2
	s_add_u32 s18, s4, s18
	v_lshl_add_u64 v[8:9], s[68:69], 0, v[6:7]
	v_mov_b32_e32 v2, v176
	v_mov_b32_e32 v3, v0
	s_addc_u32 s19, s5, s19
	global_store_dword v[8:9], v11, off
	global_store_dwordx2 v177, v[2:3], s[20:21]
	global_store_dword v177, v5, s[18:19]
	s_branch .LBB0_1621
